# v15 + 'down' expert-weight copy items of both layers moved from the router idle waves to the tail of the up GEMM phases (workgroups with one unit fewer, rank/stride from the routed block count)
# speedup vs baseline: 1.0064x; 1.0054x over previous
;     ...
;     for (int it = it0 + gw; it < it1; it += NGW) {
;         const int e = it / 384, r = it % 384; const size_t eo = (size_t)(layer * 64 + e) * 1024 * 256;
;         if (r < 128) p0_transpose_item(inp(F, I_WGATE) + eo, 1024, 256, UP + (size_t)e * 512 * 1024, 3, scr, r, F.lane);
;         else if (r < 256) p0_transpose_item(inp(F, I_WUP) + eo, 1024, 256, UP + (size_t)e * 512 * 1024, 4, scr, r - 128, F.lane);
;         else p0_transpose_item(inp(F, I_WDOWN) + eo, 256, 1024, DN + (size_t)e * 1024 * 256, 5, scr, r - 256, F.lane, 16.f);
.Lcv0_07:
	s_mul_hi_i32 s12, s5, 0x2aaaaaab
	s_lshr_b32 s13, s12, 31
	s_ashr_i32 s12, s12, 6
	s_add_i32 s12, s12, s13
	s_mul_i32 s13, s12, 0xfffffe80
	s_add_i32 s54, s5, s13
	s_ashr_i32 s13, s12, 31
	s_lshl_b64 s[14:15], s[12:13], 18
	s_add_u32 s14, s14, 0
	s_addc_u32 s15, s15, 0
	s_cmpk_gt_i32 s54, 0x7f
	s_mov_b64 s[16:17], -1
	s_cbranch_scc0 .Lcv0_13
	s_cmpk_gt_u32 s54, 0xff
	s_cbranch_scc0 .Lcv0_10
	s_branch .Lcv0_skip
; #define GAS __attribute__((address_space(1)))
; __device__ __forceinline__ unsigned pk2(float lo, float hi) { return f2bf(lo) | (f2bf(hi) << 16); }
; #define NTLD(P) (NT_STREAMS ? __builtin_nontemporal_load(P) : *(P))
;     (void)scr;
;     const int nblk = N / 32, kb = item / nblk, nb = item % nblk, a = lane & 7, q = lane >> 3, k0 = 64 * kb + 8 * q, n0 = 32 * nb + 4 * a;
;     const GAS f32x4* src = (const GAS f32x4*)(W + (size_t)k0 * N + n0);
;     f32x4 r[8];
; #pragma unroll
;     for (int i = 0; i < 8; ++i) r[i] = NTLD(src + (size_t)i * (N / 4));
; #pragma unroll
;     for (int j = 0; j < 4; ++j) { v4u o; o.x = pk2(r[0][j] * scale, r[1][j] * scale); o.y = pk2(r[2][j] * scale, r[3][j] * scale); o.z = pk2(r[4][j] * scale, r[5][j] * scale); o.w = pk2(r[6][j] * scale, r[7][j] * scale);
;         if (NT_STREAMS) __builtin_nontemporal_store(o, (GAS v4u*)(WT + (size_t)maprow(mode, n0 + j) * K + k0)); else *(GAS v4u*)(WT + (size_t)maprow(mode, n0 + j) * K + k0) = o; }
	v_mov_b32_e32 v2, s45
	ds_read_b64 v[2:3], v2
	s_lshl_b64 s[16:17], s[14:15], 2
	s_waitcnt lgkmcnt(0)
	v_readfirstlane_b32 s30, v2
	v_readfirstlane_b32 s31, v3
	s_add_u32 s16, s30, s16
	s_addc_u32 s17, s31, s17
	s_lshl_b64 s[56:57], s[12:13], 19
	s_add_u32 s56, s19, s56
	s_addc_u32 s57, s20, s57
	s_lshl_b32 s30, s12, 8
	s_sub_i32 s30, s43, s30
	s_and_b32 s30, s30, 0x1c0
	v_or_b32_e32 v42, s30, v1
	s_and_b32 s30, s23, 0x3e0
	v_or_b32_e32 v4, s30, v10
	v_lshlrev_b32_e32 v6, 12, v42
	v_lshl_add_u64 v[2:3], s[16:17], 0, v[6:7]
	v_lshlrev_b32_e32 v6, 2, v4
	v_lshl_add_u64 v[8:9], v[2:3], 0, v[6:7]
	v_add_co_u32_e32 v18, vcc, s3, v8
	global_load_dwordx4 v[2:5], v[8:9], off nt
	s_nop 0
	v_addc_co_u32_e32 v19, vcc, 0, v9, vcc
	v_add_co_u32_e32 v26, vcc, s47, v8
	global_load_dwordx4 v[14:17], v[18:19], off offset:-4096 nt
	s_nop 0
	global_load_dwordx4 v[18:21], v[18:19], off nt
	v_addc_co_u32_e32 v27, vcc, 0, v9, vcc
	v_add_co_u32_e32 v34, vcc, s48, v8
	global_load_dwordx4 v[22:25], v[26:27], off offset:-4096 nt
	s_nop 0
	global_load_dwordx4 v[26:29], v[26:27], off nt
	v_addc_co_u32_e32 v35, vcc, 0, v9, vcc
	v_add_co_u32_e32 v8, vcc, s49, v8
	global_load_dwordx4 v[30:33], v[34:35], off offset:-4096 nt
	s_nop 0
	global_load_dwordx4 v[34:37], v[34:35], off nt
	v_addc_co_u32_e32 v9, vcc, 0, v9, vcc
	global_load_dwordx4 v[38:41], v[8:9], off nt
	s_lshr_b32 s16, s54, 1
	v_lshlrev_b32_e32 v8, 1, v42
	v_and_b32_e32 v6, 0x3f0, v6
	v_mov_b32_e32 v9, v7
	v_and_or_b32 v6, s16, 12, v6
	v_lshl_add_u64 v[8:9], s[56:57], 0, v[8:9]
	v_lshlrev_b32_e32 v6, 9, v6
	v_lshl_add_u64 v[8:9], v[8:9], 0, v[6:7]
	s_mov_b64 s[16:17], 0
	s_waitcnt vmcnt(7)
	v_mov_b32_e32 v42, v2
	s_waitcnt vmcnt(6)
	v_mov_b32_e32 v44, v14
	s_waitcnt vmcnt(5)
	v_mov_b32_e32 v43, v18
	v_mov_b32_e32 v18, v3
	v_pk_mul_f32 v[2:3], v[42:43], s[4:5] op_sel_hi:[1,0]
	v_pk_mul_f32 v[18:19], v[18:19], s[4:5] op_sel_hi:[1,0]
	s_waitcnt vmcnt(4)
	v_mov_b32_e32 v45, v22
	s_waitcnt vmcnt(3)
	v_mov_b32_e32 v46, v26
	v_mov_b32_e32 v22, v15
	v_pk_mul_f32 v[14:15], v[44:45], s[4:5] op_sel_hi:[1,0]
	v_pk_mul_f32 v[22:23], v[22:23], s[4:5] op_sel_hi:[1,0]
	s_waitcnt vmcnt(2)
	v_mov_b32_e32 v48, v30
	s_waitcnt vmcnt(1)
	v_mov_b32_e32 v47, v34
	v_mov_b32_e32 v34, v27
	v_pk_mul_f32 v[26:27], v[46:47], s[4:5] op_sel_hi:[1,0]
	s_waitcnt vmcnt(0)
	v_mov_b32_e32 v49, v38
	v_mov_b32_e32 v38, v31
	v_pk_mul_f32 v[30:31], v[48:49], s[4:5] op_sel_hi:[1,0]
	v_bfe_u32 v46, v27, 16, 1
	v_bfe_u32 v47, v2, 16, 1
	v_bfe_u32 v6, v31, 16, 1
	v_bfe_u32 v44, v14, 16, 1
	v_bfe_u32 v48, v3, 16, 1
	v_add3_u32 v27, v27, v46, s50
	v_add3_u32 v2, v2, v47, s50
	v_bfe_u32 v42, v30, 16, 1
	v_bfe_u32 v43, v15, 16, 1
	v_bfe_u32 v45, v26, 16, 1
	v_add3_u32 v14, v14, v44, s50
	v_add3_u32 v6, v31, v6, s50
	v_add3_u32 v3, v3, v48, s50
	v_lshrrev_b32_e32 v27, 16, v27
	v_lshrrev_b32_e32 v2, 16, v2
	v_pk_mul_f32 v[34:35], v[34:35], s[4:5] op_sel_hi:[1,0]
	v_add3_u32 v15, v15, v43, s50
	v_add3_u32 v30, v30, v42, s50
	v_add3_u32 v26, v26, v45, s50
	v_lshrrev_b32_e32 v3, 16, v3
	v_and_or_b32 v45, v6, s51, v27
	v_and_or_b32 v42, v14, s51, v2
	v_bfe_u32 v6, v18, 16, 1
	v_bfe_u32 v14, v19, 16, 1
	v_pk_mul_f32 v[38:39], v[38:39], s[4:5] op_sel_hi:[1,0]
	v_bfe_u32 v51, v23, 16, 1
	v_bfe_u32 v52, v22, 16, 1
	v_lshrrev_b32_e32 v26, 16, v26
	v_and_or_b32 v43, v15, s51, v3
	v_bfe_u32 v2, v34, 16, 1
	v_bfe_u32 v3, v35, 16, 1
	v_add3_u32 v14, v19, v14, s50
	v_add3_u32 v6, v18, v6, s50
	v_bfe_u32 v49, v39, 16, 1
	v_bfe_u32 v50, v38, 16, 1
	v_add3_u32 v22, v22, v52, s50
	v_add3_u32 v23, v23, v51, s50
	v_and_or_b32 v44, v30, s51, v26
	v_add3_u32 v3, v35, v3, s50
	v_add3_u32 v2, v34, v2, s50
	v_lshrrev_b32_e32 v6, 16, v6
	v_lshrrev_b32_e32 v14, 16, v14
	v_add3_u32 v31, v38, v50, s50
	v_add3_u32 v38, v39, v49, s50
	global_store_dwordx4 v[8:9], v[42:45], off nt
	v_lshrrev_b32_e32 v2, 16, v2
	v_lshrrev_b32_e32 v3, 16, v3
	v_and_or_b32 v43, v23, s51, v14
	v_and_or_b32 v42, v22, s51, v6
	v_mov_b32_e32 v22, v32
	v_mov_b32_e32 v23, v40
	v_and_or_b32 v45, v38, s51, v3
	v_and_or_b32 v44, v31, s51, v2
	v_mov_b32_e32 v2, v4
	v_mov_b32_e32 v3, v20
	v_mov_b32_e32 v14, v16
	v_mov_b32_e32 v15, v24
	v_pk_mul_f32 v[22:23], v[22:23], s[4:5] op_sel_hi:[1,0]
	v_pk_mul_f32 v[2:3], v[2:3], s[4:5] op_sel_hi:[1,0]
	v_pk_mul_f32 v[14:15], v[14:15], s[4:5] op_sel_hi:[1,0]
	v_mov_b32_e32 v18, v28
	v_mov_b32_e32 v19, v36
	v_bfe_u32 v4, v23, 16, 1
	v_bfe_u32 v6, v22, 16, 1
	v_pk_mul_f32 v[18:19], v[18:19], s[4:5] op_sel_hi:[1,0]
	v_bfe_u32 v16, v15, 16, 1
	v_bfe_u32 v20, v14, 16, 1
	v_add3_u32 v6, v22, v6, s50
	v_add3_u32 v4, v23, v4, s50
	v_bfe_u32 v22, v2, 16, 1
	v_bfe_u32 v23, v3, 16, 1
	v_add3_u32 v14, v14, v20, s50
	v_add3_u32 v15, v15, v16, s50
	v_bfe_u32 v16, v18, 16, 1
	v_bfe_u32 v20, v19, 16, 1
	v_add3_u32 v3, v3, v23, s50
	v_add3_u32 v2, v2, v22, s50
	v_add3_u32 v19, v19, v20, s50
	v_add3_u32 v16, v18, v16, s50
	v_lshrrev_b32_e32 v2, 16, v2
	v_lshrrev_b32_e32 v3, 16, v3
	v_mov_b32_e32 v24, v17
	global_store_dwordx4 v[8:9], v[42:45], off offset:512 nt
	v_lshrrev_b32_e32 v16, 16, v16
	v_lshrrev_b32_e32 v18, 16, v19
	v_and_or_b32 v43, v15, s51, v3
	v_and_or_b32 v42, v14, s51, v2
	v_pk_mul_f32 v[2:3], v[24:25], s[4:5] op_sel_hi:[1,0]
	v_and_or_b32 v45, v4, s51, v18
	v_and_or_b32 v44, v6, s51, v16
	v_and_b32_sdwa v4, v3, v11 dst_sel:DWORD dst_unused:UNUSED_PAD src0_sel:WORD_1 src1_sel:DWORD
	v_and_b32_sdwa v6, v2, v11 dst_sel:DWORD dst_unused:UNUSED_PAD src0_sel:WORD_1 src1_sel:DWORD
	v_add3_u32 v3, v3, v4, s50
	v_add3_u32 v2, v2, v6, s50
	v_mov_b32_e32 v20, v5
	v_and_b32_e32 v4, 0xffff0000, v3
	v_and_b32_e32 v6, 0xffff0000, v2
	v_pk_mul_f32 v[2:3], v[20:21], s[4:5] op_sel_hi:[1,0]
	v_mov_b32_e32 v28, v33
	v_and_b32_sdwa v5, v3, v11 dst_sel:DWORD dst_unused:UNUSED_PAD src0_sel:WORD_1 src1_sel:DWORD
	v_and_b32_sdwa v14, v2, v11 dst_sel:DWORD dst_unused:UNUSED_PAD src0_sel:WORD_1 src1_sel:DWORD
	v_add3_u32 v3, v3, v5, s50
	v_add3_u32 v2, v2, v14, s50
	v_or_b32_sdwa v3, v4, v3 dst_sel:DWORD dst_unused:UNUSED_PAD src0_sel:DWORD src1_sel:WORD_1
	v_pk_mul_f32 v[4:5], v[28:29], s[4:5] op_sel_hi:[1,0]
	v_or_b32_sdwa v2, v6, v2 dst_sel:DWORD dst_unused:UNUSED_PAD src0_sel:DWORD src1_sel:WORD_1
	v_and_b32_sdwa v6, v5, v11 dst_sel:DWORD dst_unused:UNUSED_PAD src0_sel:WORD_1 src1_sel:DWORD
	v_and_b32_sdwa v14, v4, v11 dst_sel:DWORD dst_unused:UNUSED_PAD src0_sel:WORD_1 src1_sel:DWORD
	v_add3_u32 v5, v5, v6, s50
	v_mov_b32_e32 v36, v41
	v_add3_u32 v4, v4, v14, s50
	v_lshrrev_b32_e32 v5, 16, v5
	v_pk_mul_f32 v[14:15], v[36:37], s[4:5] op_sel_hi:[1,0]
	v_and_or_b32 v4, v4, s51, v5
	v_and_b32_sdwa v5, v15, v11 dst_sel:DWORD dst_unused:UNUSED_PAD src0_sel:WORD_1 src1_sel:DWORD
	v_and_b32_sdwa v6, v14, v11 dst_sel:DWORD dst_unused:UNUSED_PAD src0_sel:WORD_1 src1_sel:DWORD
	v_add3_u32 v5, v15, v5, s50
	v_add3_u32 v6, v14, v6, s50
	v_lshrrev_b32_e32 v5, 16, v5
	global_store_dwordx4 v[8:9], v[42:45], off offset:1024 nt
	v_and_or_b32 v5, v6, s51, v5
	v_lshl_add_u64 v[8:9], v[8:9], 0, s[10:11]

;     ...
;     for (int it = it0 + gw; it < it1; it += NGW) {
.Lcv0_skip:
	s_add_i32 s5, s5, s2
	s_add_i32 s21, s21, s22
	s_add_i32 s23, s23, s40
	s_add_i32 s41, s41, s42
	s_add_i32 s43, s43, s44
	s_cmpk_lt_i32 s5, 0x6000
	s_cbranch_scc1 .Lcv0_07
	s_branch .Lcv0_end

; #define LAS __attribute__((address_space(3)))
; template <class T> __device__ __forceinline__ T* wsp(const Frame& F, size_t off) { return (T*)(F.ws + off); }
; #define SEAM(k) do { if (lo <= (k) && (k) + 1 < hi) xcd_barrier(bar); } while (0)
;     LAS float* scr = (LAS float*)(F.lds + RING_OFF + F.wave * 16384);
;     const int gw = (ncu ? (int)blockIdx.x - cu0 : F.vcu) * NWAVES + F.wave, NGW = (ncu ? ncu : F.G) * NWAVES;
;     bf16* UP = wsp<bf16>(F, WS_WEUP); bf16* DN = wsp<bf16>(F, WS_WEDN);
;     for (int it = it0 + gw; it < it1; it += NGW) {
;         const int e = it / 384, r = it % 384; const size_t eo = (size_t)(layer * 64 + e) * 1024 * 256;
;         if (r < 128) p0_transpose_item(inp(F, I_WGATE) + eo, 1024, 256, UP + (size_t)e * 512 * 1024, 3, scr, r, F.lane);
;         else if (r < 256) p0_transpose_item(inp(F, I_WUP) + eo, 1024, 256, UP + (size_t)e * 512 * 1024, 4, scr, r - 128, F.lane);
;         else p0_transpose_item(inp(F, I_WDOWN) + eo, 256, 1024, DN + (size_t)e * 1024 * 256, 5, scr, r - 256, F.lane, 16.f);
; template <int LAYER, int CHUNK> __device__ __forceinline__ void moe_chunk(Frame& F, const XcdBarrier& bar, const int lo, const int hi) {
;     ...
;         moe_rows(F, rows, NBr, NBr + CT / 256, 2, list, CHUNK * CT);
;         MoeOrder<true> S{tb, NBr, NBr + CT / 256, 2, F.G, F.vcu, (unsigned)WS_HX, 1024, (unsigned)WS_WEUP, 512u * 1024u * 2u, (unsigned)WS_SHUP + (unsigned)LAYER * 512u * 1024u * 2u, 1024, list, cnt, CHUNK * CT, rows};
;     ...
;         { if (UP_DRY == 2) moe_rows(F, rows, NBr, NBr + CT / 256, 2, list, CHUNK * CT, true);
;           pg8::EpiSwiglu E{wsp<bf16>(F, WS_HID), 256, F.ws, UP_DRY == 1 ? 1 : 0}; pg8::gemm_phase(F.lds + RING_OFF, F.ws, 1024, 1024, S, E); FENCE(F);
;           if (UP_DRY == 2) { __syncthreads(); moe_rows(F, rows, NBr, NBr + CT / 256, 2, list, CHUNK * CT); } }
;     ...
;         pg8::EpiSwiglu E{wsp<bf16>(F, WS_HID), 256, F.ws}; pg8::gemm_phase(F.lds + RING_OFF, F.ws, 1024, 1024, S, E); } SEAM(p);
.Lcd0_entry:
	s_cmpk_lg_i32 s67, 0x100
	s_cbranch_scc1 .Lcd0_end
	s_add_i32 s2, 0, 0x21500
	v_mov_b32_e32 v2, s2
	ds_read_b32 v2, v2
	s_waitcnt lgkmcnt(0)
	v_readfirstlane_b32 s3, v2
	s_lshl_b32 s3, s3, 1
	s_addk_i32 s3, 0x110
	s_and_b32 s3, s3, 0xff
	s_sub_i32 s4, s71, s3
	s_cmp_lt_i32 s4, 0
	s_cbranch_scc1 .Lcd0_end
	s_sub_i32 s3, 0x100, s3
	v_mov_b32_e32 v2, v0
	s_lshl_b32 s63, s3, 3
	s_lshl_b32 s4, s4, 3
	v_readfirstlane_b32 s5, v2
	s_ashr_i32 s5, s5, 6
	s_add_i32 s62, s4, s5
	s_cmpk_gt_i32 s62, 0x13ff
	s_cbranch_scc1 .Lcd0_end
	s_movk_i32 s2, 0
	s_movk_i32 s3, 0x2000
	s_lshr_b32 s5, s62, 7
	s_add_i32 s5, s5, 24
	s_mul_i32 s5, s5, 0x180
	s_and_b32 s64, s62, 0x7f
	s_add_i32 s5, s5, s64
	s_addk_i32 s5, 0x100
	s_add_u32 s9, s38, 0x4800000
	s_addc_u32 s18, s39, 0
	s_add_u32 s19, s38, 0x2800000
	v_and_b32_e32 v1, 56, v2
	v_lshlrev_b32_e32 v2, 2, v2
	s_addc_u32 s20, s39, 0
	v_and_b32_e32 v10, 28, v2
	s_lshl_b32 s21, s5, 6
	s_lshl_b32 s22, s2, 6
	s_lshl_b32 s23, s5, 5
	s_lshl_b32 s40, s2, 5
	s_lshl_b32 s41, s5, 3
	s_lshl_b32 s42, s2, 3
	s_lshl_b32 s43, s5, 1
	s_lshl_b32 s44, s2, 1
	s_add_i32 s45, 0, 0x202a8
	s_waitcnt lgkmcnt(1)
	v_mov_b32_e32 v7, 0
	s_movk_i32 s46, 0x1000
	s_movk_i32 s47, 0x4000
	s_movk_i32 s48, 0x6000
	s_movk_i32 s49, 0x7000
	s_mov_b32 s4, 0x41800000
	s_movk_i32 s50, 0x7fff
	s_mov_b32 s51, 0xffff0000
	s_mov_b64 s[10:11], 0x600
	s_add_i32 s52, 0, 0x202a0
	s_add_i32 s53, 0, 0x20298
	v_mov_b32_e32 v11, 1
	v_mov_b32_e32 v12, 0x400
	v_mov_b32_e32 v13, 0x7c
	s_branch .Lcd0_07
.Lcd0_06:
	s_waitcnt lgkmcnt(0)
	global_store_dwordx4 v[8:9], v[2:5], off nt
	s_add_i32 s62, s62, s63
	s_cmpk_gt_i32 s62, 0x13ff
	s_cbranch_scc1 .Lcd0_end
	s_lshr_b32 s5, s62, 7
	s_add_i32 s5, s5, 24
	s_mul_i32 s5, s5, 0x180
	s_and_b32 s64, s62, 0x7f
	s_add_i32 s5, s5, s64
	s_addk_i32 s5, 0x100
	s_lshl_b32 s21, s5, 6
	s_lshl_b32 s23, s5, 5
	s_lshl_b32 s41, s5, 3
	s_lshl_b32 s43, s5, 1

;     __device__ __forceinline__ void st(const void* p, const u32x4& v) const { __builtin_amdgcn_raw_buffer_store_b128(v, r, (unsigned)((const unsigned char*)p - b), 0, EPI_SC1); }
; __device__ __forceinline__ unsigned xb_ld(unsigned* p)              { return __hip_atomic_load(p, __ATOMIC_RELAXED, __HIP_MEMORY_SCOPE_AGENT); }
; __device__ __forceinline__ void xcd_barrier_complete(unsigned* bar, unsigned x, unsigned& nloc, unsigned& nx) {
;     const unsigned G = gridDim.x * gridDim.y * gridDim.z;
;     unsigned sum, cnt, mine, sp = 0u;
;     for (;;) {
;         sum = 0u; cnt = 0u; mine = 0u;
; #pragma unroll
;         for (unsigned j = 0; j < 16; ++j) { const unsigned c = xb_ld(&bar[XB_XCNT(j)]); sum += c; cnt += (c > 0u) ? 1u : 0u; mine = (j == x) ? c : mine; }
; __device__ __forceinline__ void xcd_barrier(const XcdBarrier& b) {
;     asm volatile("s_waitcnt vmcnt(0)" ::: "memory");
;     __syncthreads();
;     if (threadIdx.x == 0) {
;         unsigned* bar = b.bar;
;         __builtin_amdgcn_s_waitcnt(0);
;         unsigned nloc = b.st[0], nx = b.st[1];
;         if (nloc == 0u) { xcd_barrier_complete(bar, b.x, nloc, nx); b.st[0] = nloc; b.st[1] = nx; }
.Lcd0_end:
.LBB0_789:
	s_cmp_gt_i32 s35, 8
	s_cselect_b64 s[2:3], -1, 0
	s_and_b64 s[0:1], s[0:1], s[2:3]
	s_andn2_b64 vcc, exec, s[0:1]
	s_cbranch_vccnz .LBB0_843
	s_waitcnt vmcnt(0)
	s_waitcnt vmcnt(0) lgkmcnt(0)
	s_barrier
	s_and_saveexec_b64 s[0:1], s[6:7]
	s_cbranch_execz .LBB0_842
	s_add_i32 s4, 0, 0x20160
	v_mov_b32_e32 v1, s4
	s_waitcnt vmcnt(0) expcnt(0) lgkmcnt(0)
	ds_read_b32 v3, v1
	s_add_i32 s4, 0, 0x20164
	v_mov_b32_e32 v1, s4
	ds_read_b32 v1, v1
	s_waitcnt lgkmcnt(1)
	v_cmp_ne_u32_e32 vcc, 0, v3
	s_cbranch_vccnz .LBB0_806
	s_load_dwordx2 s[12:13], s[92:93], 0x4
	s_add_u32 s4, s26, 0x4200
	s_addc_u32 s5, s27, 0
	s_add_u32 s10, s26, 0x4400
	s_addc_u32 s11, s27, 0
	s_waitcnt lgkmcnt(0)
	s_mul_i32 s9, s12, s67
	s_add_u32 s12, s26, 0x4500
	s_mul_i32 s9, s9, s13
	s_addc_u32 s13, s27, 0
	s_add_u32 s14, s26, 0x4600
	s_addc_u32 s15, s27, 0
	s_add_u32 s16, s26, 0x4700
	s_addc_u32 s17, s27, 0
	s_add_u32 s18, s26, 0x4800
	s_addc_u32 s19, s27, 0
	s_add_u32 s20, s26, 0x4900
	s_addc_u32 s21, s27, 0
	s_add_u32 s22, s26, 0x4a00
	s_addc_u32 s23, s27, 0
	s_add_u32 s40, s26, 0x4b00
	s_addc_u32 s41, s27, 0
	s_add_u32 s42, s26, 0x4c00
	s_addc_u32 s43, s27, 0
	s_add_u32 s44, s26, 0x4d00
	s_addc_u32 s45, s27, 0
	s_add_u32 s46, s26, 0x4e00
	s_addc_u32 s47, s27, 0
	s_add_u32 s48, s26, 0x4f00
	s_addc_u32 s49, s27, 0
	s_add_u32 s50, s26, 0x5000
	s_addc_u32 s51, s27, 0
	s_add_u32 s52, s26, 0x5100
	s_addc_u32 s53, s27, 0
	s_add_u32 s54, s26, 0x5200
	s_addc_u32 s55, s27, 0
	s_add_u32 s56, s26, 0x5300
	s_addc_u32 s57, s27, 0
	s_mov_b32 s64, 1
	v_mov_b32_e32 v17, 0
	s_branch .LBB0_794

;     ...
;     for (int it = it0 + gw; it < it1; it += NGW) {
;         const int e = it / 384, r = it % 384; const size_t eo = (size_t)(layer * 64 + e) * 1024 * 256;
;         if (r < 128) p0_transpose_item(inp(F, I_WGATE) + eo, 1024, 256, UP + (size_t)e * 512 * 1024, 3, scr, r, F.lane);
;         else if (r < 256) p0_transpose_item(inp(F, I_WUP) + eo, 1024, 256, UP + (size_t)e * 512 * 1024, 4, scr, r - 128, F.lane);
;         else p0_transpose_item(inp(F, I_WDOWN) + eo, 256, 1024, DN + (size_t)e * 1024 * 256, 5, scr, r - 256, F.lane, 16.f);
.Lcv1_07:
	s_mul_hi_i32 s12, s5, 0x2aaaaaab
	s_lshr_b32 s13, s12, 31
	s_ashr_i32 s12, s12, 6
	s_add_i32 s12, s12, s13
	s_mul_i32 s13, s12, 0xfffffe80
	s_add_i32 s54, s5, s13
	s_ashr_i32 s13, s12, 31
	s_lshl_b64 s[14:15], s[12:13], 18
	s_add_u32 s14, s14, 0x1000000
	s_addc_u32 s15, s15, 0
	s_cmpk_gt_i32 s54, 0x7f
	s_mov_b64 s[16:17], -1
	s_cbranch_scc0 .Lcv1_13
	s_cmpk_gt_u32 s54, 0xff
	s_cbranch_scc0 .Lcv1_10
	s_branch .Lcv1_skip
; #define GAS __attribute__((address_space(1)))
; __device__ __forceinline__ unsigned pk2(float lo, float hi) { return f2bf(lo) | (f2bf(hi) << 16); }
; #define NTLD(P) (NT_STREAMS ? __builtin_nontemporal_load(P) : *(P))
;     (void)scr;
;     const int nblk = N / 32, kb = item / nblk, nb = item % nblk, a = lane & 7, q = lane >> 3, k0 = 64 * kb + 8 * q, n0 = 32 * nb + 4 * a;
;     const GAS f32x4* src = (const GAS f32x4*)(W + (size_t)k0 * N + n0);
;     f32x4 r[8];
; #pragma unroll
;     for (int i = 0; i < 8; ++i) r[i] = NTLD(src + (size_t)i * (N / 4));
; #pragma unroll
;     for (int j = 0; j < 4; ++j) { v4u o; o.x = pk2(r[0][j] * scale, r[1][j] * scale); o.y = pk2(r[2][j] * scale, r[3][j] * scale); o.z = pk2(r[4][j] * scale, r[5][j] * scale); o.w = pk2(r[6][j] * scale, r[7][j] * scale);
;         if (NT_STREAMS) __builtin_nontemporal_store(o, (GAS v4u*)(WT + (size_t)maprow(mode, n0 + j) * K + k0)); else *(GAS v4u*)(WT + (size_t)maprow(mode, n0 + j) * K + k0) = o; }
	v_mov_b32_e32 v2, s45
	ds_read_b64 v[2:3], v2
	s_lshl_b64 s[16:17], s[14:15], 2
	s_waitcnt lgkmcnt(0)
	v_readfirstlane_b32 s30, v2
	v_readfirstlane_b32 s31, v3
	s_add_u32 s16, s30, s16
	s_addc_u32 s17, s31, s17
	s_lshl_b64 s[56:57], s[12:13], 19
	s_add_u32 s56, s19, s56
	s_addc_u32 s57, s20, s57
	s_lshl_b32 s30, s12, 8
	s_sub_i32 s30, s43, s30
	s_and_b32 s30, s30, 0x1c0
	v_or_b32_e32 v42, s30, v1
	s_and_b32 s30, s23, 0x3e0
	v_or_b32_e32 v4, s30, v10
	v_lshlrev_b32_e32 v6, 12, v42
	v_lshl_add_u64 v[2:3], s[16:17], 0, v[6:7]
	v_lshlrev_b32_e32 v6, 2, v4
	v_lshl_add_u64 v[8:9], v[2:3], 0, v[6:7]
	v_add_co_u32_e32 v18, vcc, s3, v8
	global_load_dwordx4 v[2:5], v[8:9], off nt
	s_nop 0
	v_addc_co_u32_e32 v19, vcc, 0, v9, vcc
	v_add_co_u32_e32 v26, vcc, s47, v8
	global_load_dwordx4 v[14:17], v[18:19], off offset:-4096 nt
	s_nop 0
	global_load_dwordx4 v[18:21], v[18:19], off nt
	v_addc_co_u32_e32 v27, vcc, 0, v9, vcc
	v_add_co_u32_e32 v34, vcc, s48, v8
	global_load_dwordx4 v[22:25], v[26:27], off offset:-4096 nt
	s_nop 0
	global_load_dwordx4 v[26:29], v[26:27], off nt
	v_addc_co_u32_e32 v35, vcc, 0, v9, vcc
	v_add_co_u32_e32 v8, vcc, s49, v8
	global_load_dwordx4 v[30:33], v[34:35], off offset:-4096 nt
	s_nop 0
	global_load_dwordx4 v[34:37], v[34:35], off nt
	v_addc_co_u32_e32 v9, vcc, 0, v9, vcc
	global_load_dwordx4 v[38:41], v[8:9], off nt
	s_lshr_b32 s16, s54, 1
	v_lshlrev_b32_e32 v8, 1, v42
	v_and_b32_e32 v6, 0x3f0, v6
	v_mov_b32_e32 v9, v7
	v_and_or_b32 v6, s16, 12, v6
	v_lshl_add_u64 v[8:9], s[56:57], 0, v[8:9]
	v_lshlrev_b32_e32 v6, 9, v6
	v_lshl_add_u64 v[8:9], v[8:9], 0, v[6:7]
	s_mov_b64 s[16:17], 0
	s_waitcnt vmcnt(7)
	v_mov_b32_e32 v42, v2
	s_waitcnt vmcnt(6)
	v_mov_b32_e32 v44, v14
	s_waitcnt vmcnt(5)
	v_mov_b32_e32 v43, v18
	v_mov_b32_e32 v18, v3
	v_pk_mul_f32 v[2:3], v[42:43], s[4:5] op_sel_hi:[1,0]
	v_pk_mul_f32 v[18:19], v[18:19], s[4:5] op_sel_hi:[1,0]
	s_waitcnt vmcnt(4)
	v_mov_b32_e32 v45, v22
	s_waitcnt vmcnt(3)
	v_mov_b32_e32 v46, v26
	v_mov_b32_e32 v22, v15
	v_pk_mul_f32 v[14:15], v[44:45], s[4:5] op_sel_hi:[1,0]
	v_pk_mul_f32 v[22:23], v[22:23], s[4:5] op_sel_hi:[1,0]
	s_waitcnt vmcnt(2)
	v_mov_b32_e32 v48, v30
	s_waitcnt vmcnt(1)
	v_mov_b32_e32 v47, v34
	v_mov_b32_e32 v34, v27
	v_pk_mul_f32 v[26:27], v[46:47], s[4:5] op_sel_hi:[1,0]
	s_waitcnt vmcnt(0)
	v_mov_b32_e32 v49, v38
	v_mov_b32_e32 v38, v31
	v_pk_mul_f32 v[30:31], v[48:49], s[4:5] op_sel_hi:[1,0]
	v_bfe_u32 v46, v27, 16, 1
	v_bfe_u32 v47, v2, 16, 1
	v_bfe_u32 v6, v31, 16, 1
	v_bfe_u32 v44, v14, 16, 1
	v_bfe_u32 v48, v3, 16, 1
	v_add3_u32 v27, v27, v46, s50
	v_add3_u32 v2, v2, v47, s50
	v_bfe_u32 v42, v30, 16, 1
	v_bfe_u32 v43, v15, 16, 1
	v_bfe_u32 v45, v26, 16, 1
	v_add3_u32 v14, v14, v44, s50
	v_add3_u32 v6, v31, v6, s50
	v_add3_u32 v3, v3, v48, s50
	v_lshrrev_b32_e32 v27, 16, v27
	v_lshrrev_b32_e32 v2, 16, v2
	v_pk_mul_f32 v[34:35], v[34:35], s[4:5] op_sel_hi:[1,0]
	v_add3_u32 v15, v15, v43, s50
	v_add3_u32 v30, v30, v42, s50
	v_add3_u32 v26, v26, v45, s50
	v_lshrrev_b32_e32 v3, 16, v3
	v_and_or_b32 v45, v6, s51, v27
	v_and_or_b32 v42, v14, s51, v2
	v_bfe_u32 v6, v18, 16, 1
	v_bfe_u32 v14, v19, 16, 1
	v_pk_mul_f32 v[38:39], v[38:39], s[4:5] op_sel_hi:[1,0]
	v_bfe_u32 v51, v23, 16, 1
	v_bfe_u32 v52, v22, 16, 1
	v_lshrrev_b32_e32 v26, 16, v26
	v_and_or_b32 v43, v15, s51, v3
	v_bfe_u32 v2, v34, 16, 1
	v_bfe_u32 v3, v35, 16, 1
	v_add3_u32 v14, v19, v14, s50
	v_add3_u32 v6, v18, v6, s50
	v_bfe_u32 v49, v39, 16, 1
	v_bfe_u32 v50, v38, 16, 1
	v_add3_u32 v22, v22, v52, s50
	v_add3_u32 v23, v23, v51, s50
	v_and_or_b32 v44, v30, s51, v26
	v_add3_u32 v3, v35, v3, s50
	v_add3_u32 v2, v34, v2, s50
	v_lshrrev_b32_e32 v6, 16, v6
	v_lshrrev_b32_e32 v14, 16, v14
	v_add3_u32 v31, v38, v50, s50
	v_add3_u32 v38, v39, v49, s50
	global_store_dwordx4 v[8:9], v[42:45], off nt
	v_lshrrev_b32_e32 v2, 16, v2
	v_lshrrev_b32_e32 v3, 16, v3
	v_and_or_b32 v43, v23, s51, v14
	v_and_or_b32 v42, v22, s51, v6
	v_mov_b32_e32 v22, v32
	v_mov_b32_e32 v23, v40
	v_and_or_b32 v45, v38, s51, v3
	v_and_or_b32 v44, v31, s51, v2
	v_mov_b32_e32 v2, v4
	v_mov_b32_e32 v3, v20
	v_mov_b32_e32 v14, v16
	v_mov_b32_e32 v15, v24
	v_pk_mul_f32 v[22:23], v[22:23], s[4:5] op_sel_hi:[1,0]
	v_pk_mul_f32 v[2:3], v[2:3], s[4:5] op_sel_hi:[1,0]
	v_pk_mul_f32 v[14:15], v[14:15], s[4:5] op_sel_hi:[1,0]
	v_mov_b32_e32 v18, v28
	v_mov_b32_e32 v19, v36
	v_bfe_u32 v4, v23, 16, 1
	v_bfe_u32 v6, v22, 16, 1
	v_pk_mul_f32 v[18:19], v[18:19], s[4:5] op_sel_hi:[1,0]
	v_bfe_u32 v16, v15, 16, 1
	v_bfe_u32 v20, v14, 16, 1
	v_add3_u32 v6, v22, v6, s50
	v_add3_u32 v4, v23, v4, s50
	v_bfe_u32 v22, v2, 16, 1
	v_bfe_u32 v23, v3, 16, 1
	v_add3_u32 v14, v14, v20, s50
	v_add3_u32 v15, v15, v16, s50
	v_bfe_u32 v16, v18, 16, 1
	v_bfe_u32 v20, v19, 16, 1
	v_add3_u32 v3, v3, v23, s50
	v_add3_u32 v2, v2, v22, s50
	v_add3_u32 v19, v19, v20, s50
	v_add3_u32 v16, v18, v16, s50
	v_lshrrev_b32_e32 v2, 16, v2
	v_lshrrev_b32_e32 v3, 16, v3
	v_mov_b32_e32 v24, v17
	global_store_dwordx4 v[8:9], v[42:45], off offset:512 nt
	v_lshrrev_b32_e32 v16, 16, v16
	v_lshrrev_b32_e32 v18, 16, v19
	v_and_or_b32 v43, v15, s51, v3
	v_and_or_b32 v42, v14, s51, v2
	v_pk_mul_f32 v[2:3], v[24:25], s[4:5] op_sel_hi:[1,0]
	v_and_or_b32 v45, v4, s51, v18
	v_and_or_b32 v44, v6, s51, v16
	v_and_b32_sdwa v4, v3, v11 dst_sel:DWORD dst_unused:UNUSED_PAD src0_sel:WORD_1 src1_sel:DWORD
	v_and_b32_sdwa v6, v2, v11 dst_sel:DWORD dst_unused:UNUSED_PAD src0_sel:WORD_1 src1_sel:DWORD
	v_add3_u32 v3, v3, v4, s50
	v_add3_u32 v2, v2, v6, s50
	v_mov_b32_e32 v20, v5
	v_and_b32_e32 v4, 0xffff0000, v3
	v_and_b32_e32 v6, 0xffff0000, v2
	v_pk_mul_f32 v[2:3], v[20:21], s[4:5] op_sel_hi:[1,0]
	v_mov_b32_e32 v28, v33
	v_and_b32_sdwa v5, v3, v11 dst_sel:DWORD dst_unused:UNUSED_PAD src0_sel:WORD_1 src1_sel:DWORD
	v_and_b32_sdwa v14, v2, v11 dst_sel:DWORD dst_unused:UNUSED_PAD src0_sel:WORD_1 src1_sel:DWORD
	v_add3_u32 v3, v3, v5, s50
	v_add3_u32 v2, v2, v14, s50
	v_or_b32_sdwa v3, v4, v3 dst_sel:DWORD dst_unused:UNUSED_PAD src0_sel:DWORD src1_sel:WORD_1
	v_pk_mul_f32 v[4:5], v[28:29], s[4:5] op_sel_hi:[1,0]
	v_or_b32_sdwa v2, v6, v2 dst_sel:DWORD dst_unused:UNUSED_PAD src0_sel:DWORD src1_sel:WORD_1
	v_and_b32_sdwa v6, v5, v11 dst_sel:DWORD dst_unused:UNUSED_PAD src0_sel:WORD_1 src1_sel:DWORD
	v_and_b32_sdwa v14, v4, v11 dst_sel:DWORD dst_unused:UNUSED_PAD src0_sel:WORD_1 src1_sel:DWORD
	v_add3_u32 v5, v5, v6, s50
	v_mov_b32_e32 v36, v41
	v_add3_u32 v4, v4, v14, s50
	v_lshrrev_b32_e32 v5, 16, v5
	v_pk_mul_f32 v[14:15], v[36:37], s[4:5] op_sel_hi:[1,0]
	v_and_or_b32 v4, v4, s51, v5
	v_and_b32_sdwa v5, v15, v11 dst_sel:DWORD dst_unused:UNUSED_PAD src0_sel:WORD_1 src1_sel:DWORD
	v_and_b32_sdwa v6, v14, v11 dst_sel:DWORD dst_unused:UNUSED_PAD src0_sel:WORD_1 src1_sel:DWORD
	v_add3_u32 v5, v15, v5, s50
	v_add3_u32 v6, v14, v6, s50
	v_lshrrev_b32_e32 v5, 16, v5
	global_store_dwordx4 v[8:9], v[42:45], off offset:1024 nt
	v_and_or_b32 v5, v6, s51, v5
	v_lshl_add_u64 v[8:9], v[8:9], 0, s[10:11]

; #define LAS __attribute__((address_space(3)))
; template <class T> __device__ __forceinline__ T* wsp(const Frame& F, size_t off) { return (T*)(F.ws + off); }
; #define SEAM(k) do { if (lo <= (k) && (k) + 1 < hi) xcd_barrier(bar); } while (0)
;     LAS float* scr = (LAS float*)(F.lds + RING_OFF + F.wave * 16384);
;     const int gw = (ncu ? (int)blockIdx.x - cu0 : F.vcu) * NWAVES + F.wave, NGW = (ncu ? ncu : F.G) * NWAVES;
;     bf16* UP = wsp<bf16>(F, WS_WEUP); bf16* DN = wsp<bf16>(F, WS_WEDN);
;     for (int it = it0 + gw; it < it1; it += NGW) {
;         const int e = it / 384, r = it % 384; const size_t eo = (size_t)(layer * 64 + e) * 1024 * 256;
;         if (r < 128) p0_transpose_item(inp(F, I_WGATE) + eo, 1024, 256, UP + (size_t)e * 512 * 1024, 3, scr, r, F.lane);
;         else if (r < 256) p0_transpose_item(inp(F, I_WUP) + eo, 1024, 256, UP + (size_t)e * 512 * 1024, 4, scr, r - 128, F.lane);
;         else p0_transpose_item(inp(F, I_WDOWN) + eo, 256, 1024, DN + (size_t)e * 1024 * 256, 5, scr, r - 256, F.lane, 16.f);
; template <int LAYER, int CHUNK> __device__ __forceinline__ void moe_chunk(Frame& F, const XcdBarrier& bar, const int lo, const int hi) {
;     ...
;         moe_rows(F, rows, NBr, NBr + CT / 256, 2, list, CHUNK * CT);
;         MoeOrder<true> S{tb, NBr, NBr + CT / 256, 2, F.G, F.vcu, (unsigned)WS_HX, 1024, (unsigned)WS_WEUP, 512u * 1024u * 2u, (unsigned)WS_SHUP + (unsigned)LAYER * 512u * 1024u * 2u, 1024, list, cnt, CHUNK * CT, rows};
;     ...
;         { if (UP_DRY == 2) moe_rows(F, rows, NBr, NBr + CT / 256, 2, list, CHUNK * CT, true);
;           pg8::EpiSwiglu E{wsp<bf16>(F, WS_HID), 256, F.ws, UP_DRY == 1 ? 1 : 0}; pg8::gemm_phase(F.lds + RING_OFF, F.ws, 1024, 1024, S, E); FENCE(F);
;           if (UP_DRY == 2) { __syncthreads(); moe_rows(F, rows, NBr, NBr + CT / 256, 2, list, CHUNK * CT); } }
;     ...
;         pg8::EpiSwiglu E{wsp<bf16>(F, WS_HID), 256, F.ws}; pg8::gemm_phase(F.lds + RING_OFF, F.ws, 1024, 1024, S, E); } SEAM(p);
.Lcd1_entry:
	s_cmpk_lg_i32 s67, 0x100
	s_cbranch_scc1 .Lcd1_end
	s_add_i32 s2, 0, 0x21500
	v_mov_b32_e32 v2, s2
	ds_read_b32 v2, v2
	s_waitcnt lgkmcnt(0)
	v_readfirstlane_b32 s3, v2
	s_lshl_b32 s3, s3, 1
	s_addk_i32 s3, 0x100
	s_and_b32 s3, s3, 0xff
	s_sub_i32 s4, s71, s3
	s_cmp_lt_i32 s4, 0
	s_cbranch_scc1 .Lcd1_end
	s_sub_i32 s3, 0x100, s3
	v_mov_b32_e32 v2, v0
	s_lshl_b32 s63, s3, 3
	s_lshl_b32 s4, s4, 3
	v_readfirstlane_b32 s5, v2
	s_ashr_i32 s5, s5, 6
	s_add_i32 s62, s4, s5
	s_cmpk_gt_i32 s62, 0x157f
	s_cbranch_scc1 .Lcd1_end
	s_movk_i32 s2, 0
	s_movk_i32 s3, 0x2000
	s_lshr_b32 s5, s62, 7
	s_add_i32 s5, s5, 21
	s_mul_i32 s5, s5, 0x180
	s_and_b32 s64, s62, 0x7f
	s_add_i32 s5, s5, s64
	s_addk_i32 s5, 0x100
	s_add_u32 s9, s38, 0x4800000
	s_addc_u32 s18, s39, 0
	s_add_u32 s19, s38, 0x2800000
	v_and_b32_e32 v1, 56, v2
	v_lshlrev_b32_e32 v2, 2, v2
	s_addc_u32 s20, s39, 0
	v_and_b32_e32 v10, 28, v2
	s_lshl_b32 s21, s5, 6
	s_lshl_b32 s22, s2, 6
	s_lshl_b32 s23, s5, 5
	s_lshl_b32 s40, s2, 5
	s_lshl_b32 s41, s5, 3
	s_lshl_b32 s42, s2, 3
	s_lshl_b32 s43, s5, 1
	s_lshl_b32 s44, s2, 1
	s_add_i32 s45, 0, 0x202a8
	s_waitcnt lgkmcnt(1)
	v_mov_b32_e32 v7, 0
	s_movk_i32 s46, 0x1000
	s_movk_i32 s47, 0x4000
	s_movk_i32 s48, 0x6000
	s_movk_i32 s49, 0x7000
	s_mov_b32 s4, 0x41800000
	s_movk_i32 s50, 0x7fff
	s_mov_b32 s51, 0xffff0000
	s_mov_b64 s[10:11], 0x600
	s_add_i32 s52, 0, 0x202a0
	s_add_i32 s53, 0, 0x20298
	v_mov_b32_e32 v11, 1
	v_mov_b32_e32 v12, 0x400
	v_mov_b32_e32 v13, 0x7c
	s_branch .Lcd1_07
.Lcd1_06:
	s_waitcnt lgkmcnt(0)
	global_store_dwordx4 v[8:9], v[2:5], off nt
	s_add_i32 s62, s62, s63
	s_cmpk_gt_i32 s62, 0x157f
	s_cbranch_scc1 .Lcd1_end
	s_lshr_b32 s5, s62, 7
	s_add_i32 s5, s5, 21
	s_mul_i32 s5, s5, 0x180
	s_and_b32 s64, s62, 0x7f
	s_add_i32 s5, s5, s64
	s_addk_i32 s5, 0x100
	s_lshl_b32 s21, s5, 6
	s_lshl_b32 s23, s5, 5
	s_lshl_b32 s41, s5, 3
	s_lshl_b32 s43, s5, 1

;     __device__ __forceinline__ void st(const void* p, const u32x4& v) const { __builtin_amdgcn_raw_buffer_store_b128(v, r, (unsigned)((const unsigned char*)p - b), 0, EPI_SC1); }
; __device__ __forceinline__ unsigned xb_ld(unsigned* p)              { return __hip_atomic_load(p, __ATOMIC_RELAXED, __HIP_MEMORY_SCOPE_AGENT); }
; __device__ __forceinline__ void xcd_barrier_complete(unsigned* bar, unsigned x, unsigned& nloc, unsigned& nx) {
;     const unsigned G = gridDim.x * gridDim.y * gridDim.z;
;     unsigned sum, cnt, mine, sp = 0u;
;     for (;;) {
;         sum = 0u; cnt = 0u; mine = 0u;
; #pragma unroll
;         for (unsigned j = 0; j < 16; ++j) { const unsigned c = xb_ld(&bar[XB_XCNT(j)]); sum += c; cnt += (c > 0u) ? 1u : 0u; mine = (j == x) ? c : mine; }
; __device__ __forceinline__ void xcd_barrier(const XcdBarrier& b) {
;     asm volatile("s_waitcnt vmcnt(0)" ::: "memory");
;     __syncthreads();
;     if (threadIdx.x == 0) {
;         unsigned* bar = b.bar;
;         __builtin_amdgcn_s_waitcnt(0);
;         unsigned nloc = b.st[0], nx = b.st[1];
;         if (nloc == 0u) { xcd_barrier_complete(bar, b.x, nloc, nx); b.st[0] = nloc; b.st[1] = nx; }
.Lcd1_end:
.LBB0_1641:
	s_cmp_gt_i32 s35, 17
	s_cselect_b64 s[2:3], -1, 0
	s_and_b64 s[0:1], s[0:1], s[2:3]
	s_andn2_b64 vcc, exec, s[0:1]
	s_cbranch_vccnz .LBB0_1695
	s_waitcnt vmcnt(0)
	s_waitcnt vmcnt(0) lgkmcnt(0)
	s_barrier
	s_and_saveexec_b64 s[0:1], s[6:7]
	s_cbranch_execz .LBB0_1694
	s_add_i32 s4, 0, 0x20160
	v_mov_b32_e32 v1, s4
	s_waitcnt vmcnt(0) expcnt(0) lgkmcnt(0)
	ds_read_b32 v3, v1
	s_add_i32 s4, 0, 0x20164
	v_mov_b32_e32 v1, s4
	ds_read_b32 v1, v1
	s_waitcnt lgkmcnt(1)
	v_cmp_ne_u32_e32 vcc, 0, v3
	s_cbranch_vccnz .LBB0_1658
	s_load_dwordx2 s[10:11], s[92:93], 0x4
	s_add_u32 s4, s26, 0x4200
	s_addc_u32 s5, s27, 0
	s_add_u32 s8, s26, 0x4400
	s_addc_u32 s9, s27, 0
	s_waitcnt lgkmcnt(0)
	s_mul_i32 s62, s10, s67
	s_add_u32 s10, s26, 0x4500
	s_mul_i32 s62, s62, s11
	s_addc_u32 s11, s27, 0
	s_add_u32 s12, s26, 0x4600
	s_addc_u32 s13, s27, 0
	s_add_u32 s14, s26, 0x4700
	s_addc_u32 s15, s27, 0
	s_add_u32 s16, s26, 0x4800
	s_addc_u32 s17, s27, 0
	s_add_u32 s18, s26, 0x4900
	s_addc_u32 s19, s27, 0
	s_add_u32 s20, s26, 0x4a00
	s_addc_u32 s21, s27, 0
	s_add_u32 s22, s26, 0x4b00
	s_addc_u32 s23, s27, 0
	s_add_u32 s40, s26, 0x4c00
	s_addc_u32 s41, s27, 0
	s_add_u32 s42, s26, 0x4d00
	s_addc_u32 s43, s27, 0
	s_add_u32 s44, s26, 0x4e00
	s_addc_u32 s45, s27, 0
	s_add_u32 s46, s26, 0x4f00
	s_addc_u32 s47, s27, 0
	s_add_u32 s48, s26, 0x5000
	s_addc_u32 s49, s27, 0
	s_add_u32 s50, s26, 0x5100
	s_addc_u32 s51, s27, 0
	s_add_u32 s52, s26, 0x5200
	s_addc_u32 s53, s27, 0
	s_add_u32 s54, s26, 0x5300
	s_addc_u32 s55, s27, 0
	s_mov_b32 s63, 1
	v_mov_b32_e32 v17, 0
	s_branch .LBB0_1646
